# scan state waves: first operands of the next chunk fetched during the current chunk (chain starts right after the barrier); dead address code dropped from the loop head; on top of transposed LDS reads
# speedup vs baseline: 1.0048x; 1.0048x over previous
.LBB0_1113:
	s_and_b64 s[0:1], s[6:7], exec
	s_mov_b32 s0, 0x3d800000
	s_cselect_b32 s0, s0, 0x3fc00000
	v_readlane_b32 s3, v255, 13
	v_lshl_or_b32 v2, s8, 7, v123
	s_lshl_b32 s1, s3, 11
	v_or_b32_e32 v188, s0, v2
	s_movk_i32 s0, 0xf800
	s_add_i32 s2, s1, 0x1000
	v_readlane_b32 s1, v255, 11
	v_writelane_b32 v255, s0, 25
	s_lshl_b32 s3, s3, 8
	v_mov_b32_e32 v2, 0
	v_writelane_b32 v255, s2, 31
	v_or_b32_e32 v189, s1, v101
	s_mov_b32 s4, 0
	v_mov_b32_e32 v190, v167
	s_mov_b32 s0, 0
	v_mov_b32_e32 v3, v2
	v_mov_b32_e32 v4, v2
	v_mov_b32_e32 v5, v2
	v_mov_b32_e32 v6, v2
	v_mov_b32_e32 v7, v2
	v_mov_b32_e32 v8, v2
	v_mov_b32_e32 v9, v2
	v_mov_b32_e32 v10, v2
	v_mov_b32_e32 v11, v2
	v_mov_b32_e32 v12, v2
	v_mov_b32_e32 v13, v2
	v_mov_b32_e32 v14, v2
	v_mov_b32_e32 v15, v2
	v_mov_b32_e32 v16, v2
	v_mov_b32_e32 v17, v2
	v_writelane_b32 v255, s3, 23
	v_readlane_b32 s14, v254, 35
	v_readlane_b32 s15, v254, 36
	s_nop 1
	s_andn2_b64 vcc, exec, s[14:15]
	s_cbranch_vccnz .Lscan_pre_skip
	v_add_u32_e32 v246, v115, v155
	v_bfe_u32 v248, v0, 4, 2
	v_mul_u32_u24_e32 v248, 0x240, v248
	v_bfe_u32 v249, v0, 2, 2
	v_mul_u32_u24_e32 v249, 0x90, v249
	v_and_b32_e32 v250, 3, v0
	v_add_u32_e32 v248, v248, v249
	v_lshl_add_u32 v248, v250, 3, v248
	v_bfe_u32 v249, v0, 6, 2
	v_mov_b32_e32 v251, v113
	v_lshl_add_u32 v250, v249, 5, v248
	v_add_u32_e32 v247, 0x1200, v246
	ds_read2_b64 v[18:21], v246 offset1:4
	ds_read2_b64 v[22:25], v246 offset0:8 offset1:12
	ds_read_b64_tr_b16 v[66:67], v250 offset:18432

.LBB0_1114:
	v_writelane_b32 v255, s0, 11
	s_and_b32 s5, s0, 1
	v_readlane_b32 s0, v254, 35
	v_readlane_b32 s1, v254, 36
	s_andn2_b64 vcc, exec, s[0:1]
	s_mov_b64 s[76:77], -1
	v_cndmask_b32_e64 v194, 0, 1, s[0:1]
	v_cmp_ne_u32_e64 s[8:9], 1, v194
	s_mul_i32 s0, s5, 0x1e00
	v_writelane_b32 v255, s8, 17
	v_writelane_b32 v255, s9, 18
	v_writelane_b32 v255, s5, 13
	s_cbranch_vccnz .LBB0_1116
	v_readlane_b32 s0, v255, 13
	s_nop 1
	s_nop 0
	s_mul_i32 s1, s0, 0x1e00
	s_lshl_b32 s0, s0, 13
	v_add_u32_e32 v252, s1, v166
	v_add_u32_e32 v253, s0, v165
	ds_read2_b64 v[68:71], v252 offset1:80
	v_cvt_pk_bf16_f32 v198, v2, v3
	v_cvt_pk_bf16_f32 v199, v4, v5
	v_cvt_pk_bf16_f32 v202, v10, v11
	v_cvt_pk_bf16_f32 v203, v12, v13
	v_cvt_pk_bf16_f32 v200, v6, v7
	v_cvt_pk_bf16_f32 v201, v8, v9
	v_cvt_pk_bf16_f32 v204, v14, v15
	v_cvt_pk_bf16_f32 v205, v16, v17
	ds_read2_b64 v[26:29], v247 offset1:4
	ds_read2_b64 v[30:33], v247 offset0:8 offset1:12
	ds_read2_b64 v[72:75], v252 offset0:160 offset1:240
	v_mfma_f32_16x16x16_bf16 v[206:209], v[18:19], v[198:199], 0
	v_mfma_f32_16x16x16_bf16 v[210:213], v[22:23], v[202:203], 0
	ds_read_b64_tr_b16 v[34:35], v248 offset:9216
	ds_read_b64_tr_b16 v[36:37], v248 offset:9248
	ds_read_b64_tr_b16 v[38:39], v248 offset:9280
	ds_read_b64_tr_b16 v[40:41], v248 offset:9312
	v_mfma_f32_16x16x16_bf16 v[206:209], v[20:21], v[200:201], v[206:209]
	v_mfma_f32_16x16x16_bf16 v[210:213], v[24:25], v[204:205], v[210:213]
	ds_read_b64_tr_b16 v[42:43], v248 offset:13824
	ds_read_b64_tr_b16 v[44:45], v248 offset:13856
	ds_read_b64_tr_b16 v[46:47], v248 offset:13888
	ds_read_b64_tr_b16 v[48:49], v248 offset:13920
	s_waitcnt lgkmcnt(11)
	v_mfma_f32_16x16x16_bf16 v[210:213], v[68:69], v[66:67], v[210:213]
	s_waitcnt lgkmcnt(10)
	v_mfma_f32_16x16x16_bf16 v[214:217], v[26:27], v[198:199], 0
	s_waitcnt lgkmcnt(9)
	v_mfma_f32_16x16x16_bf16 v[218:221], v[30:31], v[202:203], 0
	v_mfma_f32_16x16x16_bf16 v[214:217], v[28:29], v[200:201], v[214:217]
	v_mfma_f32_16x16x16_bf16 v[218:221], v[32:33], v[204:205], v[218:221]
	ds_read_b128 v[50:53], v251 offset:33792
	ds_read_b128 v[54:57], v251 offset:33856
	ds_read_b128 v[58:61], v251 offset:33920
	ds_read_b128 v[62:65], v251 offset:33984
	v_add_u32_e32 v246, 0x900, v246
	ds_read2_b64 v[76:79], v246 offset1:4
	s_waitcnt lgkmcnt(13)
	ds_read2_b64 v[80:83], v246 offset0:8 offset1:12
	v_pk_add_f32 v[206:207], v[206:207], v[210:211]
	v_pk_add_f32 v[208:209], v[208:209], v[212:213]
	v_cvt_pk_bf16_f32 v242, v206, v207
	v_cvt_pk_bf16_f32 v243, v208, v209
	s_waitcnt lgkmcnt(13)
	ds_read_b64_tr_b16 v[84:85], v250 offset:20736
	v_add_u32_e32 v252, 0xf00, v252
	s_waitcnt lgkmcnt(13)
	ds_read2_b64 v[86:89], v252 offset1:80
	v_mfma_f32_16x16x16_bf16 v[238:241], v[74:75], v[242:243], 0
	v_mfma_f32_16x16x16_bf16 v[214:217], v[70:71], v[66:67], v[214:217]
	v_mfma_f32_16x16x16_bf16 v[2:5], v[34:35], v[66:67], v[2:5]
	v_mfma_f32_16x16x16_bf16 v[6:9], v[36:37], v[66:67], v[6:9]
	s_waitcnt lgkmcnt(12)
	v_mfma_f32_16x16x16_bf16 v[10:13], v[38:39], v[66:67], v[10:13]
	v_mfma_f32_16x16x16_bf16 v[14:17], v[40:41], v[66:67], v[14:17]
	ds_read2_b64 v[90:93], v252 offset0:160 offset1:240
	v_add_u32_e32 v247, 0x900, v247
	ds_read2_b64 v[26:29], v247 offset1:4
	s_waitcnt lgkmcnt(13)
	ds_read2_b64 v[30:33], v247 offset0:8 offset1:12
	v_cvt_pk_bf16_f32 v244, -v238, -v239
	v_cvt_pk_bf16_f32 v245, -v240, -v241
	s_waitcnt lgkmcnt(13)
	ds_read_b64_tr_b16 v[34:35], v248 offset:11520
	s_waitcnt lgkmcnt(13)
	ds_read_b64_tr_b16 v[36:37], v248 offset:11552
	s_waitcnt lgkmcnt(13)
	ds_read_b64_tr_b16 v[38:39], v248 offset:11584
	s_waitcnt lgkmcnt(13)
	ds_read_b64_tr_b16 v[40:41], v248 offset:11616
	v_mfma_f32_16x16x16_bf16 v[2:5], v[42:43], v[244:245], v[2:5]
	v_mfma_f32_16x16x16_bf16 v[6:9], v[44:45], v[244:245], v[6:9]
	v_mfma_f32_16x16x16_bf16 v[10:13], v[46:47], v[244:245], v[10:13]
	v_mfma_f32_16x16x16_bf16 v[14:17], v[48:49], v[244:245], v[14:17]
	v_mfma_f32_16x16x16_bf16 v[218:221], v[72:73], v[244:245], v[218:221]
	s_waitcnt lgkmcnt(13)
	ds_read_b64_tr_b16 v[42:43], v248 offset:16128
	s_waitcnt lgkmcnt(13)
	ds_read_b64_tr_b16 v[44:45], v248 offset:16160
	s_waitcnt lgkmcnt(13)
	ds_read_b64_tr_b16 v[46:47], v248 offset:16192
	s_waitcnt lgkmcnt(13)
	ds_read_b64_tr_b16 v[48:49], v248 offset:16224
	v_pk_mul_f32 v[2:3], v[50:51], v[2:3]
	v_pk_mul_f32 v[4:5], v[52:53], v[4:5]
	v_pk_mul_f32 v[6:7], v[54:55], v[6:7]
	v_pk_mul_f32 v[8:9], v[56:57], v[8:9]
	v_pk_mul_f32 v[10:11], v[58:59], v[10:11]
	v_pk_mul_f32 v[12:13], v[60:61], v[12:13]
	v_pk_mul_f32 v[14:15], v[62:63], v[14:15]
	v_pk_mul_f32 v[16:17], v[64:65], v[16:17]
	v_pk_add_f32 v[214:215], v[214:215], v[218:219]
	v_pk_add_f32 v[216:217], v[216:217], v[220:221]
	s_waitcnt lgkmcnt(13)
	ds_write2st64_b32 v253, v214, v215 offset0:0 offset1:1
	s_waitcnt lgkmcnt(13)
	ds_write2st64_b32 v253, v216, v217 offset0:2 offset1:3
	s_waitcnt lgkmcnt(13)
	ds_read_b128 v[50:53], v251 offset:34048
	s_waitcnt lgkmcnt(13)
	ds_read_b128 v[54:57], v251 offset:34112
	s_waitcnt lgkmcnt(13)
	ds_read_b128 v[58:61], v251 offset:34176
	s_waitcnt lgkmcnt(13)
	ds_read_b128 v[62:65], v251 offset:34240
	v_cvt_pk_bf16_f32 v198, v2, v3
	v_cvt_pk_bf16_f32 v199, v4, v5
	v_cvt_pk_bf16_f32 v202, v10, v11
	v_cvt_pk_bf16_f32 v203, v12, v13
	v_cvt_pk_bf16_f32 v200, v6, v7
	v_cvt_pk_bf16_f32 v201, v8, v9
	v_cvt_pk_bf16_f32 v204, v14, v15
	v_cvt_pk_bf16_f32 v205, v16, v17
	v_add_u32_e32 v246, v115, v155
	v_bfe_u32 v248, v0, 4, 2
	v_mul_u32_u24_e32 v248, 0x240, v248
	v_bfe_u32 v249, v0, 2, 2
	v_mul_u32_u24_e32 v249, 0x90, v249
	v_and_b32_e32 v250, 3, v0
	v_add_u32_e32 v248, v248, v249
	v_lshl_add_u32 v248, v250, 3, v248
	v_bfe_u32 v249, v0, 6, 2
	v_add_u32_e32 v246, 0x8600, v246
	v_add_u32_e32 v248, 0x8600, v248
	v_add_u32_e32 v251, 0x8600, v113
	v_lshl_add_u32 v250, v249, 5, v248
	v_add_u32_e32 v247, 0x1200, v246
	s_waitcnt lgkmcnt(13)
	ds_read2_b64 v[18:21], v246 offset1:4
	s_waitcnt lgkmcnt(13)
	ds_read2_b64 v[22:25], v246 offset0:8 offset1:12
	s_waitcnt lgkmcnt(13)
	ds_read_b64_tr_b16 v[66:67], v250 offset:18432
	v_mfma_f32_16x16x16_bf16 v[206:209], v[76:77], v[198:199], 0
	v_mfma_f32_16x16x16_bf16 v[210:213], v[80:81], v[202:203], 0
	v_mfma_f32_16x16x16_bf16 v[206:209], v[78:79], v[200:201], v[206:209]
	v_mfma_f32_16x16x16_bf16 v[210:213], v[82:83], v[204:205], v[210:213]
	v_mfma_f32_16x16x16_bf16 v[210:213], v[86:87], v[84:85], v[210:213]
	v_mfma_f32_16x16x16_bf16 v[214:217], v[26:27], v[198:199], 0
	v_mfma_f32_16x16x16_bf16 v[218:221], v[30:31], v[202:203], 0
	v_mfma_f32_16x16x16_bf16 v[214:217], v[28:29], v[200:201], v[214:217]
	v_mfma_f32_16x16x16_bf16 v[218:221], v[32:33], v[204:205], v[218:221]
	s_nop 3
	v_pk_add_f32 v[206:207], v[206:207], v[210:211]
	v_pk_add_f32 v[208:209], v[208:209], v[212:213]
	v_cvt_pk_bf16_f32 v242, v206, v207
	v_cvt_pk_bf16_f32 v243, v208, v209
	s_nop 1
	v_mfma_f32_16x16x16_bf16 v[238:241], v[92:93], v[242:243], 0
	v_mfma_f32_16x16x16_bf16 v[214:217], v[88:89], v[84:85], v[214:217]
	v_mfma_f32_16x16x16_bf16 v[2:5], v[34:35], v[84:85], v[2:5]
	v_mfma_f32_16x16x16_bf16 v[6:9], v[36:37], v[84:85], v[6:9]
	s_waitcnt lgkmcnt(13)
	v_mfma_f32_16x16x16_bf16 v[10:13], v[38:39], v[84:85], v[10:13]
	v_mfma_f32_16x16x16_bf16 v[14:17], v[40:41], v[84:85], v[14:17]
	s_nop 1
	v_cvt_pk_bf16_f32 v244, -v238, -v239
	v_cvt_pk_bf16_f32 v245, -v240, -v241
	s_waitcnt lgkmcnt(11)
	s_nop 0
	v_mfma_f32_16x16x16_bf16 v[2:5], v[42:43], v[244:245], v[2:5]
	v_mfma_f32_16x16x16_bf16 v[6:9], v[44:45], v[244:245], v[6:9]
	s_waitcnt lgkmcnt(9)
	v_mfma_f32_16x16x16_bf16 v[10:13], v[46:47], v[244:245], v[10:13]
	v_mfma_f32_16x16x16_bf16 v[14:17], v[48:49], v[244:245], v[14:17]
	v_mfma_f32_16x16x16_bf16 v[218:221], v[90:91], v[244:245], v[218:221]
	s_waitcnt lgkmcnt(6)
	s_nop 1
	v_pk_mul_f32 v[2:3], v[50:51], v[2:3]
	v_pk_mul_f32 v[4:5], v[52:53], v[4:5]
	s_waitcnt lgkmcnt(5)
	v_pk_mul_f32 v[6:7], v[54:55], v[6:7]
	v_pk_mul_f32 v[8:9], v[56:57], v[8:9]
	s_waitcnt lgkmcnt(4)
	v_pk_mul_f32 v[10:11], v[58:59], v[10:11]
	v_pk_mul_f32 v[12:13], v[60:61], v[12:13]
	s_waitcnt lgkmcnt(3)
	v_pk_mul_f32 v[14:15], v[62:63], v[14:15]
	v_pk_mul_f32 v[16:17], v[64:65], v[16:17]
	v_pk_add_f32 v[214:215], v[214:215], v[218:219]
	v_pk_add_f32 v[216:217], v[216:217], v[220:221]
	ds_write2st64_b32 v253, v214, v215 offset0:16 offset1:17
	ds_write2st64_b32 v253, v216, v217 offset0:18 offset1:19
	s_branch .Lscan_join1

.LBB0_1140:
.Lscan_join1:
	s_waitcnt lgkmcnt(0)
	s_barrier
	v_readlane_b32 s0, v255, 17
	v_readlane_b32 s1, v255, 18
	s_and_b64 vcc, exec, s[0:1]
	s_mov_b64 s[76:77], -1
	s_cbranch_vccnz .LBB0_1142
	v_readlane_b32 s0, v255, 13
	s_nop 1
	s_xor_b32 s0, s0, 1
	s_mul_i32 s1, s0, 0x1e00
	s_lshl_b32 s0, s0, 13
	v_add_u32_e32 v252, s1, v166
	v_add_u32_e32 v253, s0, v165
	ds_read2_b64 v[68:71], v252 offset1:80
	v_cvt_pk_bf16_f32 v198, v2, v3
	v_cvt_pk_bf16_f32 v199, v4, v5
	v_cvt_pk_bf16_f32 v202, v10, v11
	v_cvt_pk_bf16_f32 v203, v12, v13
	v_cvt_pk_bf16_f32 v200, v6, v7
	v_cvt_pk_bf16_f32 v201, v8, v9
	v_cvt_pk_bf16_f32 v204, v14, v15
	v_cvt_pk_bf16_f32 v205, v16, v17
	ds_read2_b64 v[26:29], v247 offset1:4
	ds_read2_b64 v[30:33], v247 offset0:8 offset1:12
	ds_read2_b64 v[72:75], v252 offset0:160 offset1:240
	v_mfma_f32_16x16x16_bf16 v[206:209], v[18:19], v[198:199], 0
	v_mfma_f32_16x16x16_bf16 v[210:213], v[22:23], v[202:203], 0
	ds_read_b64_tr_b16 v[34:35], v248 offset:9216
	ds_read_b64_tr_b16 v[36:37], v248 offset:9248
	ds_read_b64_tr_b16 v[38:39], v248 offset:9280
	ds_read_b64_tr_b16 v[40:41], v248 offset:9312
	v_mfma_f32_16x16x16_bf16 v[206:209], v[20:21], v[200:201], v[206:209]
	v_mfma_f32_16x16x16_bf16 v[210:213], v[24:25], v[204:205], v[210:213]
	ds_read_b64_tr_b16 v[42:43], v248 offset:13824
	ds_read_b64_tr_b16 v[44:45], v248 offset:13856
	ds_read_b64_tr_b16 v[46:47], v248 offset:13888
	ds_read_b64_tr_b16 v[48:49], v248 offset:13920
	s_waitcnt lgkmcnt(11)
	v_mfma_f32_16x16x16_bf16 v[210:213], v[68:69], v[66:67], v[210:213]
	s_waitcnt lgkmcnt(10)
	v_mfma_f32_16x16x16_bf16 v[214:217], v[26:27], v[198:199], 0
	s_waitcnt lgkmcnt(9)
	v_mfma_f32_16x16x16_bf16 v[218:221], v[30:31], v[202:203], 0
	v_mfma_f32_16x16x16_bf16 v[214:217], v[28:29], v[200:201], v[214:217]
	v_mfma_f32_16x16x16_bf16 v[218:221], v[32:33], v[204:205], v[218:221]
	ds_read_b128 v[50:53], v251 offset:33792
	ds_read_b128 v[54:57], v251 offset:33856
	ds_read_b128 v[58:61], v251 offset:33920
	ds_read_b128 v[62:65], v251 offset:33984
	v_add_u32_e32 v246, 0x900, v246
	ds_read2_b64 v[76:79], v246 offset1:4
	s_waitcnt lgkmcnt(13)
	ds_read2_b64 v[80:83], v246 offset0:8 offset1:12
	v_pk_add_f32 v[206:207], v[206:207], v[210:211]
	v_pk_add_f32 v[208:209], v[208:209], v[212:213]
	v_cvt_pk_bf16_f32 v242, v206, v207
	v_cvt_pk_bf16_f32 v243, v208, v209
	s_waitcnt lgkmcnt(13)
	ds_read_b64_tr_b16 v[84:85], v250 offset:20736
	v_add_u32_e32 v252, 0xf00, v252
	s_waitcnt lgkmcnt(13)
	ds_read2_b64 v[86:89], v252 offset1:80
	v_mfma_f32_16x16x16_bf16 v[238:241], v[74:75], v[242:243], 0
	v_mfma_f32_16x16x16_bf16 v[214:217], v[70:71], v[66:67], v[214:217]
	v_mfma_f32_16x16x16_bf16 v[2:5], v[34:35], v[66:67], v[2:5]
	v_mfma_f32_16x16x16_bf16 v[6:9], v[36:37], v[66:67], v[6:9]
	s_waitcnt lgkmcnt(12)
	v_mfma_f32_16x16x16_bf16 v[10:13], v[38:39], v[66:67], v[10:13]
	v_mfma_f32_16x16x16_bf16 v[14:17], v[40:41], v[66:67], v[14:17]
	ds_read2_b64 v[90:93], v252 offset0:160 offset1:240
	v_add_u32_e32 v247, 0x900, v247
	ds_read2_b64 v[26:29], v247 offset1:4
	s_waitcnt lgkmcnt(13)
	ds_read2_b64 v[30:33], v247 offset0:8 offset1:12
	v_cvt_pk_bf16_f32 v244, -v238, -v239
	v_cvt_pk_bf16_f32 v245, -v240, -v241
	s_waitcnt lgkmcnt(13)
	ds_read_b64_tr_b16 v[34:35], v248 offset:11520
	s_waitcnt lgkmcnt(13)
	ds_read_b64_tr_b16 v[36:37], v248 offset:11552
	s_waitcnt lgkmcnt(13)
	ds_read_b64_tr_b16 v[38:39], v248 offset:11584
	s_waitcnt lgkmcnt(13)
	ds_read_b64_tr_b16 v[40:41], v248 offset:11616
	v_mfma_f32_16x16x16_bf16 v[2:5], v[42:43], v[244:245], v[2:5]
	v_mfma_f32_16x16x16_bf16 v[6:9], v[44:45], v[244:245], v[6:9]
	v_mfma_f32_16x16x16_bf16 v[10:13], v[46:47], v[244:245], v[10:13]
	v_mfma_f32_16x16x16_bf16 v[14:17], v[48:49], v[244:245], v[14:17]
	v_mfma_f32_16x16x16_bf16 v[218:221], v[72:73], v[244:245], v[218:221]
	s_waitcnt lgkmcnt(13)
	ds_read_b64_tr_b16 v[42:43], v248 offset:16128
	s_waitcnt lgkmcnt(13)
	ds_read_b64_tr_b16 v[44:45], v248 offset:16160
	s_waitcnt lgkmcnt(13)
	ds_read_b64_tr_b16 v[46:47], v248 offset:16192
	s_waitcnt lgkmcnt(13)
	ds_read_b64_tr_b16 v[48:49], v248 offset:16224
	v_pk_mul_f32 v[2:3], v[50:51], v[2:3]
	v_pk_mul_f32 v[4:5], v[52:53], v[4:5]
	v_pk_mul_f32 v[6:7], v[54:55], v[6:7]
	v_pk_mul_f32 v[8:9], v[56:57], v[8:9]
	v_pk_mul_f32 v[10:11], v[58:59], v[10:11]
	v_pk_mul_f32 v[12:13], v[60:61], v[12:13]
	v_pk_mul_f32 v[14:15], v[62:63], v[14:15]
	v_pk_mul_f32 v[16:17], v[64:65], v[16:17]
	v_pk_add_f32 v[214:215], v[214:215], v[218:219]
	v_pk_add_f32 v[216:217], v[216:217], v[220:221]
	s_waitcnt lgkmcnt(13)
	ds_write2st64_b32 v253, v214, v215 offset0:0 offset1:1
	s_waitcnt lgkmcnt(13)
	ds_write2st64_b32 v253, v216, v217 offset0:2 offset1:3
	s_waitcnt lgkmcnt(13)
	ds_read_b128 v[50:53], v251 offset:34048
	s_waitcnt lgkmcnt(13)
	ds_read_b128 v[54:57], v251 offset:34112
	s_waitcnt lgkmcnt(13)
	ds_read_b128 v[58:61], v251 offset:34176
	s_waitcnt lgkmcnt(13)
	ds_read_b128 v[62:65], v251 offset:34240
	v_cvt_pk_bf16_f32 v198, v2, v3
	v_cvt_pk_bf16_f32 v199, v4, v5
	v_cvt_pk_bf16_f32 v202, v10, v11
	v_cvt_pk_bf16_f32 v203, v12, v13
	v_cvt_pk_bf16_f32 v200, v6, v7
	v_cvt_pk_bf16_f32 v201, v8, v9
	v_cvt_pk_bf16_f32 v204, v14, v15
	v_cvt_pk_bf16_f32 v205, v16, v17
	v_add_u32_e32 v246, v115, v155
	v_bfe_u32 v248, v0, 4, 2
	v_mul_u32_u24_e32 v248, 0x240, v248
	v_bfe_u32 v249, v0, 2, 2
	v_mul_u32_u24_e32 v249, 0x90, v249
	v_and_b32_e32 v250, 3, v0
	v_add_u32_e32 v248, v248, v249
	v_lshl_add_u32 v248, v250, 3, v248
	v_bfe_u32 v249, v0, 6, 2
	v_add_u32_e32 v246, 0x10c00, v246
	v_add_u32_e32 v248, 0x10c00, v248
	v_add_u32_e32 v251, 0x10c00, v113
	v_lshl_add_u32 v250, v249, 5, v248
	v_add_u32_e32 v247, 0x1200, v246
	s_waitcnt lgkmcnt(13)
	ds_read2_b64 v[18:21], v246 offset1:4
	s_waitcnt lgkmcnt(13)
	ds_read2_b64 v[22:25], v246 offset0:8 offset1:12
	s_waitcnt lgkmcnt(13)
	ds_read_b64_tr_b16 v[66:67], v250 offset:18432
	v_mfma_f32_16x16x16_bf16 v[206:209], v[76:77], v[198:199], 0
	v_mfma_f32_16x16x16_bf16 v[210:213], v[80:81], v[202:203], 0
	v_mfma_f32_16x16x16_bf16 v[206:209], v[78:79], v[200:201], v[206:209]
	v_mfma_f32_16x16x16_bf16 v[210:213], v[82:83], v[204:205], v[210:213]
	v_mfma_f32_16x16x16_bf16 v[210:213], v[86:87], v[84:85], v[210:213]
	v_mfma_f32_16x16x16_bf16 v[214:217], v[26:27], v[198:199], 0
	v_mfma_f32_16x16x16_bf16 v[218:221], v[30:31], v[202:203], 0
	v_mfma_f32_16x16x16_bf16 v[214:217], v[28:29], v[200:201], v[214:217]
	v_mfma_f32_16x16x16_bf16 v[218:221], v[32:33], v[204:205], v[218:221]
	s_nop 3
	v_pk_add_f32 v[206:207], v[206:207], v[210:211]
	v_pk_add_f32 v[208:209], v[208:209], v[212:213]
	v_cvt_pk_bf16_f32 v242, v206, v207
	v_cvt_pk_bf16_f32 v243, v208, v209
	s_nop 1
	v_mfma_f32_16x16x16_bf16 v[238:241], v[92:93], v[242:243], 0
	v_mfma_f32_16x16x16_bf16 v[214:217], v[88:89], v[84:85], v[214:217]
	v_mfma_f32_16x16x16_bf16 v[2:5], v[34:35], v[84:85], v[2:5]
	v_mfma_f32_16x16x16_bf16 v[6:9], v[36:37], v[84:85], v[6:9]
	s_waitcnt lgkmcnt(13)
	v_mfma_f32_16x16x16_bf16 v[10:13], v[38:39], v[84:85], v[10:13]
	v_mfma_f32_16x16x16_bf16 v[14:17], v[40:41], v[84:85], v[14:17]
	s_nop 1
	v_cvt_pk_bf16_f32 v244, -v238, -v239
	v_cvt_pk_bf16_f32 v245, -v240, -v241
	s_waitcnt lgkmcnt(11)
	s_nop 0
	v_mfma_f32_16x16x16_bf16 v[2:5], v[42:43], v[244:245], v[2:5]
	v_mfma_f32_16x16x16_bf16 v[6:9], v[44:45], v[244:245], v[6:9]
	s_waitcnt lgkmcnt(9)
	v_mfma_f32_16x16x16_bf16 v[10:13], v[46:47], v[244:245], v[10:13]
	v_mfma_f32_16x16x16_bf16 v[14:17], v[48:49], v[244:245], v[14:17]
	v_mfma_f32_16x16x16_bf16 v[218:221], v[90:91], v[244:245], v[218:221]
	s_waitcnt lgkmcnt(6)
	s_nop 1
	v_pk_mul_f32 v[2:3], v[50:51], v[2:3]
	v_pk_mul_f32 v[4:5], v[52:53], v[4:5]
	s_waitcnt lgkmcnt(5)
	v_pk_mul_f32 v[6:7], v[54:55], v[6:7]
	v_pk_mul_f32 v[8:9], v[56:57], v[8:9]
	s_waitcnt lgkmcnt(4)
	v_pk_mul_f32 v[10:11], v[58:59], v[10:11]
	v_pk_mul_f32 v[12:13], v[60:61], v[12:13]
	s_waitcnt lgkmcnt(3)
	v_pk_mul_f32 v[14:15], v[62:63], v[14:15]
	v_pk_mul_f32 v[16:17], v[64:65], v[16:17]
	v_pk_add_f32 v[214:215], v[214:215], v[218:219]
	v_pk_add_f32 v[216:217], v[216:217], v[220:221]
	ds_write2st64_b32 v253, v214, v215 offset0:16 offset1:17
	ds_write2st64_b32 v253, v216, v217 offset0:18 offset1:19
	s_branch .Lscan_join2

.LBB0_1160:
.Lscan_join2:
	s_waitcnt lgkmcnt(0)
	s_barrier
	v_readlane_b32 s0, v255, 17
	v_readlane_b32 s1, v255, 18
	s_and_b64 vcc, exec, s[0:1]
	s_mov_b64 s[30:31], -1
	s_cbranch_vccnz .LBB0_1162
	v_readlane_b32 s0, v255, 13
	s_nop 1
	s_nop 0
	s_mul_i32 s1, s0, 0x1e00
	s_lshl_b32 s0, s0, 13
	v_add_u32_e32 v252, s1, v166
	v_add_u32_e32 v253, s0, v165
	ds_read2_b64 v[68:71], v252 offset1:80
	v_cvt_pk_bf16_f32 v198, v2, v3
	v_cvt_pk_bf16_f32 v199, v4, v5
	v_cvt_pk_bf16_f32 v202, v10, v11
	v_cvt_pk_bf16_f32 v203, v12, v13
	v_cvt_pk_bf16_f32 v200, v6, v7
	v_cvt_pk_bf16_f32 v201, v8, v9
	v_cvt_pk_bf16_f32 v204, v14, v15
	v_cvt_pk_bf16_f32 v205, v16, v17
	ds_read2_b64 v[26:29], v247 offset1:4
	ds_read2_b64 v[30:33], v247 offset0:8 offset1:12
	ds_read2_b64 v[72:75], v252 offset0:160 offset1:240
	v_mfma_f32_16x16x16_bf16 v[206:209], v[18:19], v[198:199], 0
	v_mfma_f32_16x16x16_bf16 v[210:213], v[22:23], v[202:203], 0
	ds_read_b64_tr_b16 v[34:35], v248 offset:9216
	ds_read_b64_tr_b16 v[36:37], v248 offset:9248
	ds_read_b64_tr_b16 v[38:39], v248 offset:9280
	ds_read_b64_tr_b16 v[40:41], v248 offset:9312
	v_mfma_f32_16x16x16_bf16 v[206:209], v[20:21], v[200:201], v[206:209]
	v_mfma_f32_16x16x16_bf16 v[210:213], v[24:25], v[204:205], v[210:213]
	ds_read_b64_tr_b16 v[42:43], v248 offset:13824
	ds_read_b64_tr_b16 v[44:45], v248 offset:13856
	ds_read_b64_tr_b16 v[46:47], v248 offset:13888
	ds_read_b64_tr_b16 v[48:49], v248 offset:13920
	s_waitcnt lgkmcnt(11)
	v_mfma_f32_16x16x16_bf16 v[210:213], v[68:69], v[66:67], v[210:213]
	s_waitcnt lgkmcnt(10)
	v_mfma_f32_16x16x16_bf16 v[214:217], v[26:27], v[198:199], 0
	s_waitcnt lgkmcnt(9)
	v_mfma_f32_16x16x16_bf16 v[218:221], v[30:31], v[202:203], 0
	v_mfma_f32_16x16x16_bf16 v[214:217], v[28:29], v[200:201], v[214:217]
	v_mfma_f32_16x16x16_bf16 v[218:221], v[32:33], v[204:205], v[218:221]
	ds_read_b128 v[50:53], v251 offset:33792
	ds_read_b128 v[54:57], v251 offset:33856
	ds_read_b128 v[58:61], v251 offset:33920
	ds_read_b128 v[62:65], v251 offset:33984
	v_add_u32_e32 v246, 0x900, v246
	ds_read2_b64 v[76:79], v246 offset1:4
	s_waitcnt lgkmcnt(13)
	ds_read2_b64 v[80:83], v246 offset0:8 offset1:12
	v_pk_add_f32 v[206:207], v[206:207], v[210:211]
	v_pk_add_f32 v[208:209], v[208:209], v[212:213]
	v_cvt_pk_bf16_f32 v242, v206, v207
	v_cvt_pk_bf16_f32 v243, v208, v209
	s_waitcnt lgkmcnt(13)
	ds_read_b64_tr_b16 v[84:85], v250 offset:20736
	v_add_u32_e32 v252, 0xf00, v252
	s_waitcnt lgkmcnt(13)
	ds_read2_b64 v[86:89], v252 offset1:80
	v_mfma_f32_16x16x16_bf16 v[238:241], v[74:75], v[242:243], 0
	v_mfma_f32_16x16x16_bf16 v[214:217], v[70:71], v[66:67], v[214:217]
	v_mfma_f32_16x16x16_bf16 v[2:5], v[34:35], v[66:67], v[2:5]
	v_mfma_f32_16x16x16_bf16 v[6:9], v[36:37], v[66:67], v[6:9]
	s_waitcnt lgkmcnt(12)
	v_mfma_f32_16x16x16_bf16 v[10:13], v[38:39], v[66:67], v[10:13]
	v_mfma_f32_16x16x16_bf16 v[14:17], v[40:41], v[66:67], v[14:17]
	ds_read2_b64 v[90:93], v252 offset0:160 offset1:240
	v_add_u32_e32 v247, 0x900, v247
	ds_read2_b64 v[26:29], v247 offset1:4
	s_waitcnt lgkmcnt(13)
	ds_read2_b64 v[30:33], v247 offset0:8 offset1:12
	v_cvt_pk_bf16_f32 v244, -v238, -v239
	v_cvt_pk_bf16_f32 v245, -v240, -v241
	s_waitcnt lgkmcnt(13)
	ds_read_b64_tr_b16 v[34:35], v248 offset:11520
	s_waitcnt lgkmcnt(13)
	ds_read_b64_tr_b16 v[36:37], v248 offset:11552
	s_waitcnt lgkmcnt(13)
	ds_read_b64_tr_b16 v[38:39], v248 offset:11584
	s_waitcnt lgkmcnt(13)
	ds_read_b64_tr_b16 v[40:41], v248 offset:11616
	v_mfma_f32_16x16x16_bf16 v[2:5], v[42:43], v[244:245], v[2:5]
	v_mfma_f32_16x16x16_bf16 v[6:9], v[44:45], v[244:245], v[6:9]
	v_mfma_f32_16x16x16_bf16 v[10:13], v[46:47], v[244:245], v[10:13]
	v_mfma_f32_16x16x16_bf16 v[14:17], v[48:49], v[244:245], v[14:17]
	v_mfma_f32_16x16x16_bf16 v[218:221], v[72:73], v[244:245], v[218:221]
	s_waitcnt lgkmcnt(13)
	ds_read_b64_tr_b16 v[42:43], v248 offset:16128
	s_waitcnt lgkmcnt(13)
	ds_read_b64_tr_b16 v[44:45], v248 offset:16160
	s_waitcnt lgkmcnt(13)
	ds_read_b64_tr_b16 v[46:47], v248 offset:16192
	s_waitcnt lgkmcnt(13)
	ds_read_b64_tr_b16 v[48:49], v248 offset:16224
	v_pk_mul_f32 v[2:3], v[50:51], v[2:3]
	v_pk_mul_f32 v[4:5], v[52:53], v[4:5]
	v_pk_mul_f32 v[6:7], v[54:55], v[6:7]
	v_pk_mul_f32 v[8:9], v[56:57], v[8:9]
	v_pk_mul_f32 v[10:11], v[58:59], v[10:11]
	v_pk_mul_f32 v[12:13], v[60:61], v[12:13]
	v_pk_mul_f32 v[14:15], v[62:63], v[14:15]
	v_pk_mul_f32 v[16:17], v[64:65], v[16:17]
	v_pk_add_f32 v[214:215], v[214:215], v[218:219]
	v_pk_add_f32 v[216:217], v[216:217], v[220:221]
	s_waitcnt lgkmcnt(13)
	ds_write2st64_b32 v253, v214, v215 offset0:0 offset1:1
	s_waitcnt lgkmcnt(13)
	ds_write2st64_b32 v253, v216, v217 offset0:2 offset1:3
	s_waitcnt lgkmcnt(13)
	ds_read_b128 v[50:53], v251 offset:34048
	s_waitcnt lgkmcnt(13)
	ds_read_b128 v[54:57], v251 offset:34112
	s_waitcnt lgkmcnt(13)
	ds_read_b128 v[58:61], v251 offset:34176
	s_waitcnt lgkmcnt(13)
	ds_read_b128 v[62:65], v251 offset:34240
	v_cvt_pk_bf16_f32 v198, v2, v3
	v_cvt_pk_bf16_f32 v199, v4, v5
	v_cvt_pk_bf16_f32 v202, v10, v11
	v_cvt_pk_bf16_f32 v203, v12, v13
	v_cvt_pk_bf16_f32 v200, v6, v7
	v_cvt_pk_bf16_f32 v201, v8, v9
	v_cvt_pk_bf16_f32 v204, v14, v15
	v_cvt_pk_bf16_f32 v205, v16, v17
	v_add_u32_e32 v246, v115, v155
	v_bfe_u32 v248, v0, 4, 2
	v_mul_u32_u24_e32 v248, 0x240, v248
	v_bfe_u32 v249, v0, 2, 2
	v_mul_u32_u24_e32 v249, 0x90, v249
	v_and_b32_e32 v250, 3, v0
	v_add_u32_e32 v248, v248, v249
	v_lshl_add_u32 v248, v250, 3, v248
	v_bfe_u32 v249, v0, 6, 2
	v_mov_b32_e32 v251, v113
	v_lshl_add_u32 v250, v249, 5, v248
	v_add_u32_e32 v247, 0x1200, v246
	s_waitcnt lgkmcnt(13)
	ds_read2_b64 v[18:21], v246 offset1:4
	s_waitcnt lgkmcnt(13)
	ds_read2_b64 v[22:25], v246 offset0:8 offset1:12
	s_waitcnt lgkmcnt(13)
	ds_read_b64_tr_b16 v[66:67], v250 offset:18432
	v_mfma_f32_16x16x16_bf16 v[206:209], v[76:77], v[198:199], 0
	v_mfma_f32_16x16x16_bf16 v[210:213], v[80:81], v[202:203], 0
	v_mfma_f32_16x16x16_bf16 v[206:209], v[78:79], v[200:201], v[206:209]
	v_mfma_f32_16x16x16_bf16 v[210:213], v[82:83], v[204:205], v[210:213]
	v_mfma_f32_16x16x16_bf16 v[210:213], v[86:87], v[84:85], v[210:213]
	v_mfma_f32_16x16x16_bf16 v[214:217], v[26:27], v[198:199], 0
	v_mfma_f32_16x16x16_bf16 v[218:221], v[30:31], v[202:203], 0
	v_mfma_f32_16x16x16_bf16 v[214:217], v[28:29], v[200:201], v[214:217]
	v_mfma_f32_16x16x16_bf16 v[218:221], v[32:33], v[204:205], v[218:221]
	s_nop 3
	v_pk_add_f32 v[206:207], v[206:207], v[210:211]
	v_pk_add_f32 v[208:209], v[208:209], v[212:213]
	v_cvt_pk_bf16_f32 v242, v206, v207
	v_cvt_pk_bf16_f32 v243, v208, v209
	s_nop 1
	v_mfma_f32_16x16x16_bf16 v[238:241], v[92:93], v[242:243], 0
	v_mfma_f32_16x16x16_bf16 v[214:217], v[88:89], v[84:85], v[214:217]
	v_mfma_f32_16x16x16_bf16 v[2:5], v[34:35], v[84:85], v[2:5]
	v_mfma_f32_16x16x16_bf16 v[6:9], v[36:37], v[84:85], v[6:9]
	s_waitcnt lgkmcnt(13)
	v_mfma_f32_16x16x16_bf16 v[10:13], v[38:39], v[84:85], v[10:13]
	v_mfma_f32_16x16x16_bf16 v[14:17], v[40:41], v[84:85], v[14:17]
	s_nop 1
	v_cvt_pk_bf16_f32 v244, -v238, -v239
	v_cvt_pk_bf16_f32 v245, -v240, -v241
	s_waitcnt lgkmcnt(11)
	s_nop 0
	v_mfma_f32_16x16x16_bf16 v[2:5], v[42:43], v[244:245], v[2:5]
	v_mfma_f32_16x16x16_bf16 v[6:9], v[44:45], v[244:245], v[6:9]
	s_waitcnt lgkmcnt(9)
	v_mfma_f32_16x16x16_bf16 v[10:13], v[46:47], v[244:245], v[10:13]
	v_mfma_f32_16x16x16_bf16 v[14:17], v[48:49], v[244:245], v[14:17]
	v_mfma_f32_16x16x16_bf16 v[218:221], v[90:91], v[244:245], v[218:221]
	s_waitcnt lgkmcnt(6)
	s_nop 1
	v_pk_mul_f32 v[2:3], v[50:51], v[2:3]
	v_pk_mul_f32 v[4:5], v[52:53], v[4:5]
	s_waitcnt lgkmcnt(5)
	v_pk_mul_f32 v[6:7], v[54:55], v[6:7]
	v_pk_mul_f32 v[8:9], v[56:57], v[8:9]
	s_waitcnt lgkmcnt(4)
	v_pk_mul_f32 v[10:11], v[58:59], v[10:11]
	v_pk_mul_f32 v[12:13], v[60:61], v[12:13]
	s_waitcnt lgkmcnt(3)
	v_pk_mul_f32 v[14:15], v[62:63], v[14:15]
	v_pk_mul_f32 v[16:17], v[64:65], v[16:17]
	v_pk_add_f32 v[214:215], v[214:215], v[218:219]
	v_pk_add_f32 v[216:217], v[216:217], v[220:221]
	ds_write2st64_b32 v253, v214, v215 offset0:16 offset1:17
	ds_write2st64_b32 v253, v216, v217 offset0:18 offset1:19
	s_branch .Lscan_join3

.LBB0_1186:
.Lscan_join3:
	s_waitcnt lgkmcnt(0)
	s_barrier
	v_readlane_b32 s5, v255, 11
	v_readlane_b32 s1, v255, 25
	s_add_i32 s0, s5, 3
	s_addk_i32 s4, 0x60
	s_addk_i32 s1, 0x1800
	v_writelane_b32 v255, s1, 25
	s_cmpk_gt_u32 s5, 0x44
	v_add_u32_e32 v190, 0xffffffa0, v190
	s_cbranch_scc1 .LBB0_1188
	s_branch .LBB0_1114
	v_mov_b32_e32 v2, v18
	v_mov_b32_e32 v3, v19
	v_mov_b32_e32 v4, v20
	v_mov_b32_e32 v5, v21
	v_mov_b32_e32 v6, v22
	v_mov_b32_e32 v7, v23
	v_mov_b32_e32 v8, v24
	v_mov_b32_e32 v9, v25
	v_mov_b32_e32 v10, v26
	v_mov_b32_e32 v11, v27
	v_mov_b32_e32 v12, v28
	v_mov_b32_e32 v13, v29
	v_mov_b32_e32 v14, v30
	v_mov_b32_e32 v15, v31
	v_mov_b32_e32 v16, v32
	v_mov_b32_e32 v17, v33
	s_branch .LBB0_1114
